# batch 3 plus N1: one expert-counter reservation (returning atomic) per workgroup and layer instead of one per 16-row block; list entries parked in LDS and written after the block loop
# speedup vs baseline: 1.0049x; 1.0049x over previous
; #define LAS __attribute__((address_space(3)))
; DI unsigned pk2(float lo, float hi) { f32x2 v = {lo, hi}; bf16x2v r = __builtin_convertvector(v, bf16x2v); return __builtin_bit_cast(unsigned, r); }
; DI const float* inp(kptr_t k, int i) { return (const float*)k[i]; }
; DI void phase_n1(Frame& F, int l) {
;     ...
;     const float* wr_ = inp(KA, I_WROUTER) + (size_t)l * D * NE;
;     for (int idx = F.tid; idx < D * 8; idx += 512) { const int k = idx >> 3, c = idx & 7; const f32x4 v = *(const f32x4*)(wr_ + k * 32 + 4 * c);
; #pragma unroll
;         for (int q = 0; q < 4; ++q) *(LAS bf16_t*)(WTl + (4 * c + q) * RP + k * 2) = (bf16_t)(pk2(v[q], 0.f) & 0xffffu); }
;     __syncthreads();
;     const float* mod = (const float*)(F.ws + WS_MOD) + (size_t)l * NB * NMOD * D;
;     const bf16_t* ymix = (const bf16_t*)(F.ws + WS_YMIX); unsigned char* h8 = F.ws + WS_H8;
;     const float* xin = inp(KA, I_X); bf16_t* xb = (bf16_t*)(F.ws + WS_XB);
;     int2* lists = (int2*)(F.ws + WS_LISTS); unsigned* cntg = F.ctl + CW_CNT + l * NE * 64;
;     const float brt = inp(KA, I_BROUTER)[l * NE + (F.lane & 31)];
;     for (int blk = F.bid; blk < T / 16; blk += F.G) {
;         if (F.tid < 32) hist[F.tid] = 0;
;         f32x4 hv[2][4], yv2[2][4], xv2[2][4];
; #pragma unroll
;         for (int rr = 0; rr < 2; ++rr) { const int r = blk * 16 + F.wave * 2 + rr;
;             load_row_bf16(ymix + (size_t)r * D, F.lane, yv2[rr]); if (l == 0) load_row_f32(xin + (size_t)r * D, F.lane, xv2[rr]); else load_row_bf16(xb + (size_t)r * D, F.lane, xv2[rr]); }
.LBB0_1027:
	s_or_b64 exec, exec, s[2:3]
	v_readlane_b32 s0, v255, 14
	s_lshl_b32 s42, s0, 11
	s_cmpk_gt_i32 s30, 0x7ff
	s_waitcnt lgkmcnt(0)
	s_barrier
	v_readlane_b32 s1, v255, 15
	s_cbranch_scc1 .LBB0_1128
	s_load_dwordx2 s[0:1], s[20:21], 0xb8
	v_readlane_b32 s2, v255, 14
	v_and_b32_e32 v146, 31, v2
	s_mov_b32 s6, s2
	v_readlane_b32 s3, v255, 15
	v_lshl_or_b32 v0, s6, 5, v146
	s_load_dwordx2 s[2:3], s[20:21], 0x0
	s_waitcnt lgkmcnt(0)
	v_lshl_add_u64 v[4:5], v[0:1], 2, s[0:1]
	global_load_dword v0, v[4:5], off
	s_mul_i32 s0, s6, 0x60000
	v_readlane_b32 s1, v253, 13
	s_add_u32 s31, s1, s0
	v_readlane_b32 s0, v253, 14
	s_mov_b32 s43, s59
	s_addc_u32 s33, s0, 0
	s_lshl_b64 s[0:1], s[42:43], 2
	v_readlane_b32 s4, v253, 55
	v_readlane_b32 s5, v253, 56
	s_add_u32 s0, s4, s0
	s_addc_u32 s1, s5, s1
	s_lshl_b32 s58, s6, 10
	v_lshlrev_b32_e32 v8, 2, v3
	v_readlane_b32 s6, v254, 0
	v_lshlrev_b32_e32 v4, 2, v2
	v_ashrrev_i32_e32 v5, 31, v4
	v_add_u32_e32 v147, s6, v8
	v_readlane_b32 s6, v253, 49
	v_lshlrev_b64 v[6:7], 1, v[4:5]
	v_readlane_b32 s7, v253, 50
	v_lshl_add_u64 v[102:103], v[4:5], 2, s[2:3]
	v_readlane_b32 s2, v253, 19
	v_lshl_add_u64 v[98:99], s[6:7], 0, v[6:7]
	v_readlane_b32 s6, v253, 51
	v_readlane_b32 s7, v253, 52
	v_readlane_b32 s3, v253, 20
	v_and_b32_e32 v9, -16, v2
	v_lshl_add_u64 v[100:101], s[6:7], 0, v[6:7]
	v_lshl_add_u64 v[104:105], s[2:3], 0, v[4:5]
	s_mul_i32 s2, s97, 0x1020
	v_readlane_b32 s6, v254, 1
	v_lshlrev_b32_e32 v6, 3, v2
	v_and_b32_e32 v7, 15, v2
	v_lshlrev_b32_e32 v12, 5, v2
	v_ashrrev_i32_e32 v14, 5, v2
	v_lshlrev_b32_e32 v2, 6, v3
	v_cmp_gt_i32_e64 s[4:5], 32, v3
	s_add_i32 s2, s6, s2
	v_mov_b32_e32 v10, s6
	s_movk_i32 s6, 0x810
	v_ashrrev_i32_e32 v3, 31, v2
	v_mad_u32_u24 v10, v7, s6, v10
	v_mad_u32_u24 v11, v7, s6, 0
	s_lshl_b32 s6, s97, 11
	v_readlane_b32 s7, v254, 2
	v_lshl_add_u64 v[106:107], v[2:3], 2, s[0:1]
	v_readlane_b32 s0, v254, 3
	s_lshl_b32 s3, s97, 8
	s_add_i32 s6, s6, s7
	v_add_u32_e32 v149, s0, v8
	s_lshl_b32 s0, s97, 3
	s_lshl_b32 s1, s30, 6
	s_lshl_b32 s14, s97, 1
	v_add_u32_e32 v9, s3, v9
	v_and_b32_e32 v12, 0xfffffe00, v12
	v_lshl_add_u32 v7, v7, 2, s6
	v_add_u32_e32 v13, s7, v4
	s_add_i32 s1, s1, s0
	v_lshlrev_b32_e32 v2, 2, v14
	s_lshl_b32 s0, s30, 4
	v_xor_b32_e32 v148, 64, v4
	v_cmp_gt_u32_e64 s[6:7], 4, v146
	v_cmp_eq_u32_e64 s[8:9], 0, v146
	v_cmp_eq_u32_e64 s[10:11], 1, v146
	v_cmp_eq_u32_e64 s[12:13], 2, v146
	v_add3_u32 v108, s1, v2, v146
	s_add_i32 s22, s0, s14
	s_lshl_b64 s[24:25], s[58:59], 2
	v_lshlrev_b64 v[110:111], 2, v[4:5]
	v_add_u32_e32 v150, s2, v6
	v_add_u32_e32 v151, v10, v9
	v_add_u32_e32 v152, v11, v9
	v_add_u32_e32 v153, v7, v12
	v_add_u32_e32 v154, s3, v13
	s_mov_b32 s100, 0
	v_mbcnt_lo_u32_b32 v206, -1, 0
	v_mbcnt_hi_u32_b32 v206, -1, v206
	v_lshrrev_b32_e32 v207, 5, v206
	v_and_b32_e32 v206, 3, v206
	v_lshl_add_u32 v206, v207, 2, v206
	s_lshl_b32 s101, s97, 3
	v_add_u32_e32 v206, s101, v206
	v_lshlrev_b32_e32 v206, 4, v206
	v_add_u32_e32 v206, 0x1d000, v206
	s_branch .LBB0_1030
.LBB0_1029:
	s_or_b64 exec, exec, s[2:3]
	s_add_i32 s30, s30, s72
	s_add_i32 s22, s22, s38
	s_add_i32 s100, s100, 1
	s_cmpk_lt_i32 s30, 0x800
	v_add_u32_e32 v108, s48, v108
	s_cbranch_scc0 .LBB0_1128
.LBB0_1030:
	s_cmp_lg_u32 s100, 0
	s_cbranch_scc1 .Ln1_nozero
	s_and_saveexec_b64 s[2:3], s[4:5]
	ds_write_b32 v147, v1
	s_or_b64 exec, exec, s[2:3]
.Ln1_nozero:
	s_ashr_i32 s23, s22, 31
	s_lshl_b64 s[28:29], s[22:23], 11
	v_lshl_add_u64 v[2:3], v[98:99], 0, s[28:29]
	global_load_dwordx2 v[24:25], v[2:3], off nt
	global_load_dwordx2 v[22:23], v[2:3], off offset:512 nt
	global_load_dwordx2 v[20:21], v[2:3], off offset:1024 nt
	global_load_dwordx2 v[18:19], v[2:3], off offset:1536 nt
	v_readlane_b32 s0, v253, 23
	v_readlane_b32 s1, v253, 24
	s_lshl_b64 s[26:27], s[22:23], 10
	s_mov_b64 s[2:3], -1
	s_and_b64 vcc, exec, s[0:1]
	s_cbranch_vccz .LBB0_1034
	v_lshl_add_u64 v[2:3], s[26:27], 1, v[100:101]
	global_load_dwordx2 v[4:5], v[2:3], off nt
	global_load_dwordx2 v[6:7], v[2:3], off offset:512 nt
	global_load_dwordx2 v[8:9], v[2:3], off offset:1024 nt
	s_nop 0
	global_load_dwordx2 v[2:3], v[2:3], off offset:1536 nt
	s_mov_b64 s[2:3], 0
	s_waitcnt vmcnt(0)
	v_lshlrev_b32_e32 v62, 16, v4
	v_and_b32_e32 v63, 0xffff0000, v4
	v_lshlrev_b32_e32 v64, 16, v5
	v_and_b32_e32 v65, 0xffff0000, v5
	v_lshlrev_b32_e32 v58, 16, v6
	v_and_b32_e32 v59, 0xffff0000, v6
	v_lshlrev_b32_e32 v60, 16, v7
	v_and_b32_e32 v61, 0xffff0000, v7
	v_lshlrev_b32_e32 v50, 16, v8
	v_and_b32_e32 v51, 0xffff0000, v8
	v_lshlrev_b32_e32 v52, 16, v9
	v_and_b32_e32 v53, 0xffff0000, v9
	v_lshlrev_b32_e32 v38, 16, v2
	v_and_b32_e32 v39, 0xffff0000, v2
	v_lshlrev_b32_e32 v40, 16, v3
	v_and_b32_e32 v41, 0xffff0000, v3

; DI void phase_n1(Frame& F, int l) {
;     ...
;         const float e1 = __expf(topv[1] - topv[0]), e2 = __expf(topv[2] - topv[0]), e3 = __expf(topv[3] - topv[0]); const float inv = 1.0f / (1.0f + e1 + e2 + e3);
;         const int ks = F.lane & 31; const bool slot = ks < 4;
;         const int my_e = ks == 0 ? tope[0] : (ks == 1 ? tope[1] : (ks == 2 ? tope[2] : tope[3]));
;         const float my_g = (ks == 0 ? 1.0f : (ks == 1 ? e1 : (ks == 2 ? e2 : e3))) * inv;
;         const int row = blk * 16 + F.wave * 2 + (F.lane >> 5);
;         __syncthreads();
;         int lrank = 0; if (slot) lrank = atomicAdd((int*)(hist + my_e), 1);
;         __syncthreads();
;         if (F.tid < 32) { const int n = hist[F.tid]; basew[F.tid] = n ? (int)atomicAdd(cntg + F.tid * 64, (unsigned)n) : 0; }
;         __syncthreads();
;         if (slot) { const int pos = basew[my_e] + lrank; int2 ent; ent.x = row * 4 + ks; ent.y = __float_as_int(my_g); lists[(size_t)my_e * LIST_CAP + pos] = ent; }
.LBB0_1120:
	s_or_b64 exec, exec, s[14:15]
	v_cndmask_b32_e64 v7, v9, v7, s[12:13]
	v_cndmask_b32_e64 v5, v7, v5, s[10:11]
	v_cndmask_b32_e64 v2, v5, v2, s[8:9]
	v_mov_b32_e32 v5, 0
	s_waitcnt lgkmcnt(0)
	s_barrier
	s_and_saveexec_b64 s[2:3], s[6:7]
	v_lshl_add_u32 v5, v2, 2, 0
	v_add_u32_e32 v5, 0x20100, v5
	v_mov_b32_e32 v7, 1
	ds_add_rtn_u32 v5, v5, v7
	s_or_b64 exec, exec, s[2:3]
	v_sub_f32_e32 v4, v4, v3
	v_sub_f32_e32 v6, v6, v3
	v_sub_f32_e32 v3, v8, v3
	v_mul_f32_e32 v4, 0x3fb8aa3b, v4
	v_mul_f32_e32 v6, 0x3fb8aa3b, v6
	v_mul_f32_e32 v3, 0x3fb8aa3b, v3
	v_exp_f32_e32 v4, v4
	v_exp_f32_e32 v6, v6
	v_exp_f32_e32 v3, v3
	s_waitcnt lgkmcnt(0)
	s_and_saveexec_b64 s[2:3], s[6:7]
	s_cbranch_execz .LBB0_1029
	v_add_f32_e32 v7, 1.0, v4
	v_add_f32_e32 v7, v7, v6
	v_add_f32_e32 v7, v7, v3
	v_div_scale_f32 v8, s[0:1], v7, v7, 1.0
	v_rcp_f32_e32 v9, v8
	v_div_scale_f32 v10, vcc, 1.0, v7, 1.0
	v_cndmask_b32_e64 v3, v3, v6, s[12:13]
	v_fma_f32 v11, -v8, v9, 1.0
	v_fmac_f32_e32 v9, v11, v9
	v_mul_f32_e32 v11, v10, v9
	v_fma_f32 v12, -v8, v11, v10
	v_fmac_f32_e32 v11, v12, v9
	v_fma_f32 v8, -v8, v11, v10
	v_div_fmas_f32 v8, v8, v9, v11
	v_cndmask_b32_e64 v3, v3, v4, s[10:11]
	v_div_fixup_f32 v7, v8, v7, 1.0
	v_cndmask_b32_e64 v3, v3, 1.0, s[8:9]
	v_mul_f32_e32 v109, v7, v3
	v_mov_b32_e32 v208, v2
	v_mov_b32_e32 v209, v5
	v_mov_b32_e32 v210, v108
	v_mov_b32_e32 v211, v109
	s_lshl_b32 s101, s100, 10
	v_add_u32_e32 v207, s101, v206
	ds_write_b128 v207, v[208:211]
	s_branch .LBB0_1029
.LBB0_1128:
	s_waitcnt lgkmcnt(0)
	s_barrier
	s_and_saveexec_b64 s[2:3], s[4:5]
	s_cbranch_execz .Ln1_fin1
	ds_read_b32 v9, v147
	v_mov_b32_e32 v7, 0
	s_waitcnt lgkmcnt(0)
	v_cmp_ne_u32_e32 vcc, 0, v9
	s_and_saveexec_b64 s[14:15], vcc
	s_cbranch_execz .Ln1_fin0
	global_atomic_add v7, v[106:107], v9, off sc0

; DI void phase_n1(Frame& F, int l) {
;     ...
;         int lrank = 0; if (slot) lrank = atomicAdd((int*)(hist + my_e), 1);
;         __syncthreads();
;         if (F.tid < 32) { const int n = hist[F.tid]; basew[F.tid] = n ? (int)atomicAdd(cntg + F.tid * 64, (unsigned)n) : 0; }
;         __syncthreads();
;         if (slot) { const int pos = basew[my_e] + lrank; int2 ent; ent.x = row * 4 + ks; ent.y = __float_as_int(my_g); lists[(size_t)my_e * LIST_CAP + pos] = ent; }
;     }
;     __syncthreads();
.Ln1_fin1:
	s_or_b64 exec, exec, s[2:3]
	s_waitcnt lgkmcnt(0)
	s_barrier
	s_and_saveexec_b64 s[2:3], s[6:7]
	s_cbranch_execz .Ln1_fin3
	v_readlane_b32 s0, v253, 53
	v_readlane_b32 s1, v253, 54
	s_mov_b32 s101, 0
.Ln1_fin2:
	s_lshl_b32 s14, s101, 10
	v_add_u32_e32 v207, s14, v206
	ds_read_b128 v[208:211], v207
	s_waitcnt lgkmcnt(0)
	v_lshl_add_u32 v6, v208, 2, 0
	v_add_u32_e32 v6, 0x20180, v6
	ds_read_b32 v6, v6
	v_mov_b32_e32 v2, v208
	v_ashrrev_i32_e32 v3, 31, v2
	v_lshlrev_b64 v[2:3], 18, v[2:3]
	v_lshl_add_u64 v[2:3], s[0:1], 0, v[2:3]
	s_waitcnt lgkmcnt(0)
	v_add_u32_e32 v4, v6, v209
	v_ashrrev_i32_e32 v5, 31, v4
	v_lshl_add_u64 v[2:3], v[4:5], 3, v[2:3]
	global_store_dwordx2 v[2:3], v[210:211], off
	s_add_i32 s101, s101, 1
	s_cmp_lt_u32 s101, s100
	s_cbranch_scc1 .Ln1_fin2
.Ln1_fin3:
	s_or_b64 exec, exec, s[2:3]
	v_readlane_b32 s2, v253, 2
	s_mov_b32 s0, s94
	v_readlane_b32 s3, v253, 3
	s_mov_b32 s1, -1
	s_barrier
	v_readlane_b32 s4, v253, 29
	v_mbcnt_lo_u32_b32 v0, s1, 0
	v_mbcnt_hi_u32_b32 v0, s1, v0
	s_mov_b32 s33, s4
	s_waitcnt vmcnt(0)
	v_readlane_b32 s5, v253, 30
	v_lshl_add_u32 v4, s97, 6, v0
	v_cmp_eq_u32_e64 s[4:5], 0, v4
	s_barrier
	s_and_saveexec_b64 s[56:57], s[4:5]
	s_cbranch_execz .LBB0_1172
	s_add_i32 s1, 0, 0x20000
	v_mov_b32_e32 v0, s1
	s_waitcnt vmcnt(0) expcnt(0) lgkmcnt(0)
	ds_read_b32 v2, v0
	v_mov_b32_e32 v0, s73
	ds_read_b32 v0, v0
	s_waitcnt lgkmcnt(1)
	v_cmp_ne_u32_e32 vcc, 0, v2
	s_cbranch_vccnz .LBB0_1143
	v_readlane_b32 s6, v253, 0
	v_readlane_b32 s7, v253, 1
	s_load_dwordx2 s[10:11], s[6:7], 0x4
	s_add_u32 s6, s2, 0x1000
	s_addc_u32 s7, s3, 0
	s_add_u32 s8, s2, 0x1100
	s_addc_u32 s9, s3, 0
	s_waitcnt lgkmcnt(0)
	s_mul_i32 s34, s10, s72
	s_add_u32 s10, s2, 0x1200
	s_mul_i32 s34, s34, s11
	s_addc_u32 s11, s3, 0
	s_add_u32 s12, s2, 0x1300
	s_addc_u32 s13, s3, 0
	s_mov_b32 s35, 1
	s_mov_b64 s[14:15], 0
	s_branch .LBB0_1133
